# MoE phase prologues: unit-table loads (moe_fill) issued together instead of one exposed round trip each; plus earlier de-serialized epilogue chains, scans, lists
# speedup vs baseline: 1.0248x; 1.0069x over previous
.LBB0_1070:
	v_readlane_b32 s8, v252, 1
	v_readlane_b32 s10, v252, 3
	s_cmp_le_i32 s10, s12
	s_cselect_b64 s[4:5], -1, 0
	s_and_b64 s[4:5], s[4:5], s[6:7]
	s_andn2_b64 vcc, exec, s[4:5]
	v_readlane_b32 s9, v252, 2
	v_readlane_b32 s11, v252, 4
	s_cbranch_vccnz .LBB0_1203
	v_readlane_b32 s6, v252, 6
	v_mbcnt_lo_u32_b32 v0, -1, 0
	v_mbcnt_hi_u32_b32 v0, -1, v0
	v_readlane_b32 s20, v252, 0
	v_readlane_b32 s7, v252, 7
	s_load_dwordx2 s[48:49], s[6:7], 0xe0
	v_mov_b32_e32 v2, 0x401000
	s_and_b32 s6, s20, 7
	s_ashr_i32 s18, s20, 3
	s_ashr_i32 s7, s20, 31
	s_waitcnt lgkmcnt(0)
	global_load_dword v2, v2, s[48:49]
	v_readlane_b32 s8, v253, 60
	s_mul_i32 s21, s6, s8
	s_lshr_b32 s6, s18, 30
	s_lshr_b32 s7, s7, 30
	s_add_i32 s12, s18, s6
	s_add_i32 s6, s20, s7
	s_ashr_i32 s54, s12, 2
	s_ashr_i32 s46, s6, 2
	v_readlane_b32 s6, v253, 56
	s_add_i32 s21, s21, s54
	v_readlane_b32 s7, v253, 57
	s_waitcnt vmcnt(0)
	v_readfirstlane_b32 s27, v2
	s_add_i32 s30, s27, 64
	s_and_b64 s[6:7], s[6:7], exec
	s_cselect_b32 s6, s21, s46
	v_readlane_b32 s7, v252, 10
	s_cmp_ge_i32 s6, s30
	s_nop 0
	v_add_u32_e32 v0, s7, v0
	s_cbranch_scc1 .LBB0_1176
	s_add_u32 s44, s48, 0x400000
	s_addc_u32 s45, s49, 0
	s_sub_i32 s7, s6, s27
	s_addk_i32 s7, 0x240
	s_cmp_lt_i32 s6, s27
	v_cmp_eq_u32_e64 s[38:39], 0, v0
	s_cselect_b32 s8, s6, s7
	s_and_saveexec_b64 s[6:7], s[38:39]
	s_cbranch_execz .LBB0_1074
	s_ashr_i32 s9, s8, 31
	s_lshl_b64 s[10:11], s[8:9], 2
	s_add_u32 s10, s44, s10
	s_addc_u32 s11, s45, s11
	global_load_dword v64, v1, s[10:11]
	s_add_i32 s9, 0, 0x23000
	v_mov_b32_e32 v3, s9
.LBB0_1074:
	s_or_b64 exec, exec, s[6:7]
	s_add_u32 s6, s48, 0x300000
	s_addc_u32 s7, s49, 0
	s_add_i32 s9, 0, 0x20000
	v_lshl_add_u32 v2, v0, 2, s9
	s_movk_i32 s9, 0x100
	v_cmp_gt_i32_e64 s[40:41], s9, v0
	s_and_saveexec_b64 s[10:11], s[40:41]
	s_cbranch_execz .LBB0_1076
	v_lshl_add_u32 v4, s8, 8, v0
	v_ashrrev_i32_e32 v5, 31, v4
	v_lshl_add_u64 v[4:5], v[4:5], 2, s[6:7]
	global_load_dword v80, v[4:5], off

.LBB0_1081:
	s_sub_i32 s8, s10, s27
	s_addk_i32 s8, 0x240
	s_cmp_lt_i32 s10, s27
	s_cselect_b32 s8, s10, s8
	s_and_saveexec_b64 s[10:11], s[38:39]
	s_cbranch_execz .LBB0_1083
	s_ashr_i32 s9, s8, 31
	s_lshl_b64 s[50:51], s[8:9], 2
	s_add_u32 s50, s44, s50
	s_addc_u32 s51, s45, s51
	global_load_dword v65, v1, s[50:51]
	v_readlane_b32 s9, v254, 35
	s_nop 1
	v_mov_b32_e32 v4, s9
	s_or_b64 exec, exec, s[10:11]
	s_and_saveexec_b64 s[10:11], s[40:41]
	s_cbranch_execz .LBB0_1085
	s_branch .LBB0_1084

.LBB0_1084:
	v_lshl_add_u32 v4, s8, 8, v0
	v_ashrrev_i32_e32 v5, 31, v4
	v_lshl_add_u64 v[4:5], v[4:5], 2, s[6:7]
	global_load_dword v81, v[4:5], off

.LBB0_1090:
	s_sub_i32 s8, s10, s27
	s_addk_i32 s8, 0x240
	s_cmp_lt_i32 s10, s27
	s_cselect_b32 s8, s10, s8
	s_and_saveexec_b64 s[10:11], s[38:39]
	s_cbranch_execz .LBB0_1092
	s_ashr_i32 s9, s8, 31
	s_lshl_b64 s[50:51], s[8:9], 2
	s_add_u32 s50, s44, s50
	s_addc_u32 s51, s45, s51
	global_load_dword v66, v1, s[50:51]
	v_readlane_b32 s9, v254, 36
	s_nop 1
	v_mov_b32_e32 v4, s9
	s_or_b64 exec, exec, s[10:11]
	s_and_saveexec_b64 s[10:11], s[40:41]
	s_cbranch_execz .LBB0_1094
	s_branch .LBB0_1093

.LBB0_1093:
	v_lshl_add_u32 v4, s8, 8, v0
	v_ashrrev_i32_e32 v5, 31, v4
	v_lshl_add_u64 v[4:5], v[4:5], 2, s[6:7]
	global_load_dword v82, v[4:5], off

.LBB0_1099:
	s_sub_i32 s8, s10, s27
	s_addk_i32 s8, 0x240
	s_cmp_lt_i32 s10, s27
	s_cselect_b32 s8, s10, s8
	s_and_saveexec_b64 s[10:11], s[38:39]
	s_cbranch_execz .LBB0_1101
	s_ashr_i32 s9, s8, 31
	s_lshl_b64 s[50:51], s[8:9], 2
	s_add_u32 s50, s44, s50
	s_addc_u32 s51, s45, s51
	global_load_dword v67, v1, s[50:51]
	v_readlane_b32 s9, v254, 37
	s_nop 1
	v_mov_b32_e32 v4, s9
	s_or_b64 exec, exec, s[10:11]
	s_and_saveexec_b64 s[10:11], s[40:41]
	s_cbranch_execz .LBB0_1103
	s_branch .LBB0_1102

.LBB0_1102:
	v_lshl_add_u32 v4, s8, 8, v0
	v_ashrrev_i32_e32 v5, 31, v4
	v_lshl_add_u64 v[4:5], v[4:5], 2, s[6:7]
	global_load_dword v83, v[4:5], off

.LBB0_1108:
	s_sub_i32 s8, s10, s27
	s_addk_i32 s8, 0x240
	s_cmp_lt_i32 s10, s27
	s_cselect_b32 s8, s10, s8
	s_and_saveexec_b64 s[10:11], s[38:39]
	s_cbranch_execz .LBB0_1110
	s_ashr_i32 s9, s8, 31
	s_lshl_b64 s[50:51], s[8:9], 2
	s_add_u32 s50, s44, s50
	s_addc_u32 s51, s45, s51
	global_load_dword v68, v1, s[50:51]
	v_readlane_b32 s9, v254, 38
	s_nop 1
	v_mov_b32_e32 v4, s9
	s_or_b64 exec, exec, s[10:11]
	s_and_saveexec_b64 s[10:11], s[40:41]
	s_cbranch_execz .LBB0_1112
	s_branch .LBB0_1111

.LBB0_1111:
	v_lshl_add_u32 v4, s8, 8, v0
	v_ashrrev_i32_e32 v5, 31, v4
	v_lshl_add_u64 v[4:5], v[4:5], 2, s[6:7]
	global_load_dword v84, v[4:5], off

.LBB0_1117:
	s_sub_i32 s8, s10, s27
	s_addk_i32 s8, 0x240
	s_cmp_lt_i32 s10, s27
	s_cselect_b32 s8, s10, s8
	s_and_saveexec_b64 s[10:11], s[38:39]
	s_cbranch_execz .LBB0_1119
	s_ashr_i32 s9, s8, 31
	s_lshl_b64 s[50:51], s[8:9], 2
	s_add_u32 s50, s44, s50
	s_addc_u32 s51, s45, s51
	global_load_dword v69, v1, s[50:51]
	v_readlane_b32 s9, v254, 39
	s_nop 1
	v_mov_b32_e32 v4, s9
	s_or_b64 exec, exec, s[10:11]
	s_and_saveexec_b64 s[10:11], s[40:41]
	s_cbranch_execz .LBB0_1121
	s_branch .LBB0_1120

.LBB0_1120:
	v_lshl_add_u32 v4, s8, 8, v0
	v_ashrrev_i32_e32 v5, 31, v4
	v_lshl_add_u64 v[4:5], v[4:5], 2, s[6:7]
	global_load_dword v85, v[4:5], off

.LBB0_1126:
	s_sub_i32 s8, s10, s27
	s_addk_i32 s8, 0x240
	s_cmp_lt_i32 s10, s27
	s_cselect_b32 s8, s10, s8
	s_and_saveexec_b64 s[10:11], s[38:39]
	s_cbranch_execz .LBB0_1128
	s_ashr_i32 s9, s8, 31
	s_lshl_b64 s[50:51], s[8:9], 2
	s_add_u32 s50, s44, s50
	s_addc_u32 s51, s45, s51
	global_load_dword v70, v1, s[50:51]
	v_readlane_b32 s9, v254, 40
	s_nop 1
	v_mov_b32_e32 v4, s9
	s_or_b64 exec, exec, s[10:11]
	s_and_saveexec_b64 s[10:11], s[40:41]
	s_cbranch_execz .LBB0_1130
	s_branch .LBB0_1129

.LBB0_1129:
	v_lshl_add_u32 v4, s8, 8, v0
	v_ashrrev_i32_e32 v5, 31, v4
	v_lshl_add_u64 v[4:5], v[4:5], 2, s[6:7]
	global_load_dword v86, v[4:5], off

.LBB0_1135:
	s_sub_i32 s8, s10, s27
	s_addk_i32 s8, 0x240
	s_cmp_lt_i32 s10, s27
	s_cselect_b32 s8, s10, s8
	s_and_saveexec_b64 s[10:11], s[38:39]
	s_cbranch_execz .LBB0_1137
	s_ashr_i32 s9, s8, 31
	s_lshl_b64 s[50:51], s[8:9], 2
	s_add_u32 s50, s44, s50
	s_addc_u32 s51, s45, s51
	global_load_dword v71, v1, s[50:51]
	v_readlane_b32 s9, v254, 41
	s_nop 1
	v_mov_b32_e32 v4, s9
	s_or_b64 exec, exec, s[10:11]
	s_and_saveexec_b64 s[10:11], s[40:41]
	s_cbranch_execz .LBB0_1139
	s_branch .LBB0_1138

.LBB0_1138:
	v_lshl_add_u32 v4, s8, 8, v0
	v_ashrrev_i32_e32 v5, 31, v4
	v_lshl_add_u64 v[4:5], v[4:5], 2, s[6:7]
	global_load_dword v87, v[4:5], off

.LBB0_1144:
	s_sub_i32 s8, s10, s27
	s_addk_i32 s8, 0x240
	s_cmp_lt_i32 s10, s27
	s_cselect_b32 s8, s10, s8
	s_and_saveexec_b64 s[10:11], s[38:39]
	s_cbranch_execz .LBB0_1146
	s_ashr_i32 s9, s8, 31
	s_lshl_b64 s[50:51], s[8:9], 2
	s_add_u32 s50, s44, s50
	s_addc_u32 s51, s45, s51
	global_load_dword v72, v1, s[50:51]
	v_readlane_b32 s9, v254, 42
	s_nop 1
	v_mov_b32_e32 v4, s9
	s_or_b64 exec, exec, s[10:11]
	s_and_saveexec_b64 s[10:11], s[40:41]
	s_cbranch_execz .LBB0_1148
	s_branch .LBB0_1147

.LBB0_1147:
	v_lshl_add_u32 v4, s8, 8, v0
	v_ashrrev_i32_e32 v5, 31, v4
	v_lshl_add_u64 v[4:5], v[4:5], 2, s[6:7]
	global_load_dword v88, v[4:5], off

.LBB0_1153:
	s_sub_i32 s8, s10, s27
	s_addk_i32 s8, 0x240
	s_cmp_lt_i32 s10, s27
	s_cselect_b32 s8, s10, s8
	s_and_saveexec_b64 s[10:11], s[38:39]
	s_cbranch_execz .LBB0_1155
	s_ashr_i32 s9, s8, 31
	s_lshl_b64 s[50:51], s[8:9], 2
	s_add_u32 s50, s44, s50
	s_addc_u32 s51, s45, s51
	global_load_dword v73, v1, s[50:51]
	v_readlane_b32 s9, v254, 43
	s_nop 1
	v_mov_b32_e32 v4, s9
	s_or_b64 exec, exec, s[10:11]
	s_and_saveexec_b64 s[10:11], s[40:41]
	s_cbranch_execz .LBB0_1157
	s_branch .LBB0_1156

.LBB0_1156:
	v_lshl_add_u32 v4, s8, 8, v0
	v_ashrrev_i32_e32 v5, 31, v4
	v_lshl_add_u64 v[4:5], v[4:5], 2, s[6:7]
	global_load_dword v89, v[4:5], off

.LBB0_1162:
	s_sub_i32 s8, s10, s27
	s_addk_i32 s8, 0x240
	s_cmp_lt_i32 s10, s27
	s_cselect_b32 s8, s10, s8
	s_and_saveexec_b64 s[10:11], s[38:39]
	s_cbranch_execz .LBB0_1164
	s_ashr_i32 s9, s8, 31
	s_lshl_b64 s[50:51], s[8:9], 2
	s_add_u32 s50, s44, s50
	s_addc_u32 s51, s45, s51
	global_load_dword v74, v1, s[50:51]
	v_readlane_b32 s9, v254, 44
	s_nop 1
	v_mov_b32_e32 v4, s9
	s_or_b64 exec, exec, s[10:11]
	s_and_saveexec_b64 s[10:11], s[40:41]
	s_cbranch_execz .LBB0_1166
	s_branch .LBB0_1165

.LBB0_1165:
	v_lshl_add_u32 v4, s8, 8, v0
	v_ashrrev_i32_e32 v5, 31, v4
	v_lshl_add_u64 v[4:5], v[4:5], 2, s[6:7]
	global_load_dword v90, v[4:5], off

.LBB0_1171:
	s_sub_i32 s8, s10, s27
	s_addk_i32 s8, 0x240
	s_cmp_lt_i32 s10, s27
	s_cselect_b32 s8, s10, s8
	s_and_saveexec_b64 s[10:11], s[38:39]
	s_cbranch_execz .LBB0_1173
	s_ashr_i32 s9, s8, 31
	s_lshl_b64 s[38:39], s[8:9], 2
	s_add_u32 s38, s44, s38
	s_addc_u32 s39, s45, s39
	global_load_dword v75, v1, s[38:39]
	v_readlane_b32 s9, v254, 45
	s_nop 1
	v_mov_b32_e32 v4, s9
.LBB0_1173:
	s_or_b64 exec, exec, s[10:11]
	s_and_saveexec_b64 s[10:11], s[40:41]
	s_cbranch_execz .LBB0_1175
	v_lshl_add_u32 v4, s8, 8, v0
	v_ashrrev_i32_e32 v5, 31, v4
	v_lshl_add_u64 v[4:5], v[4:5], 2, s[6:7]
	global_load_dword v91, v[4:5], off

.LBB0_1176:
	s_waitcnt vmcnt(0)
	v_lshlrev_b32_e32 v97, 2, v0
	v_add_u32_e32 v97, 0x20000, v97
	v_cmp_gt_u32_e32 vcc, 0x100, v0
	s_and_saveexec_b64 s[100:101], vcc
	ds_write_b32 v97, v80
	ds_write_b32 v97, v81 offset:1024
	ds_write_b32 v97, v82 offset:2048
	ds_write_b32 v97, v83 offset:3072
	ds_write_b32 v97, v84 offset:4096
	ds_write_b32 v97, v85 offset:5120
	ds_write_b32 v97, v86 offset:6144
	ds_write_b32 v97, v87 offset:7168
	ds_write_b32 v97, v88 offset:8192
	ds_write_b32 v97, v89 offset:9216
	ds_write_b32 v97, v90 offset:10240
	ds_write_b32 v97, v91 offset:11264
	s_mov_b64 exec, s[100:101]
	v_cmp_eq_u32_e32 vcc, 0, v0
	s_and_saveexec_b64 s[100:101], vcc
	v_mov_b32_e32 v96, 0x23000
	ds_write_b32 v96, v64
	ds_write_b32 v96, v65 offset:4
	ds_write_b32 v96, v66 offset:8
	ds_write_b32 v96, v67 offset:12
	ds_write_b32 v96, v68 offset:16
	ds_write_b32 v96, v69 offset:20
	ds_write_b32 v96, v70 offset:24
	ds_write_b32 v96, v71 offset:28
	ds_write_b32 v96, v72 offset:32
	ds_write_b32 v96, v73 offset:36
	ds_write_b32 v96, v74 offset:40
	ds_write_b32 v96, v75 offset:44
	s_mov_b64 exec, s[100:101]
	v_readlane_b32 s10, v253, 58
	v_readlane_b32 s11, v253, 59
	s_waitcnt lgkmcnt(0)
	s_barrier
	s_movk_i32 s6, 0x800
	v_readfirstlane_b32 s38, v0
	s_mov_b64 s[8:9], -1
	s_and_b64 vcc, exec, s[10:11]
	s_cbranch_vccz .LBB0_1179
	s_lshl_b32 s7, s46, 2
	s_sub_i32 s44, s20, s7
	s_cbranch_execz .LBB0_1180

.LBB0_1255:
	v_readlane_b32 s8, v252, 1
	v_readlane_b32 s10, v252, 3
	s_cmp_le_i32 s10, s12
	s_cselect_b64 s[4:5], -1, 0
	s_and_b64 s[4:5], s[4:5], s[6:7]
	s_andn2_b64 vcc, exec, s[4:5]
	v_readlane_b32 s9, v252, 2
	v_readlane_b32 s11, v252, 4
	s_cbranch_vccnz .LBB0_1298
	v_mbcnt_lo_u32_b32 v0, -1, 0
	v_mbcnt_hi_u32_b32 v0, -1, v0
	v_readlane_b32 s20, v252, 0
	v_readlane_b32 s6, v252, 10
	s_mov_b32 s10, 0
	s_mov_b32 s11, s20
	v_add_u32_e32 v14, s6, v0
	v_readlane_b32 s6, v252, 6
	v_readlane_b32 s7, v252, 7
	s_load_dwordx2 s[44:45], s[6:7], 0xe0
	v_mov_b32_e32 v0, 0x401000
	v_readlane_b32 s7, v253, 60
	v_cmp_eq_u32_e64 s[38:39], 0, v14
	s_waitcnt lgkmcnt(0)
	global_load_dword v0, v0, s[44:45]
	s_add_u32 s8, s44, 0x400000
	s_addc_u32 s9, s45, 0
	s_and_b32 s6, s20, 7
	s_mul_i32 s30, s6, s7
	s_ashr_i32 s6, s20, 5
	s_add_i32 s30, s30, s6
	s_mov_b32 s12, s30
	s_waitcnt vmcnt(0)
	v_readfirstlane_b32 s21, v0
	s_add_i32 s27, s21, 64
	s_mov_b32 s100, 0
	s_branch .LBB0_1259

.LBB0_1261:
	s_cmp_ge_i32 s18, s27
	s_mov_b64 s[6:7], -1
	s_cbranch_scc1 .LBB0_1258
	s_and_saveexec_b64 s[6:7], s[38:39]
	s_cbranch_execz .LBB0_1264
	s_sub_i32 s42, s18, s21
	s_addk_i32 s42, 0x240
	s_cmp_lt_i32 s18, s21
	s_cselect_b32 s42, s18, s42
	s_ashr_i32 s43, s42, 31
	s_lshl_b64 s[42:43], s[42:43], 2
	s_lshr_b32 s101, s10, 2
	s_add_i32 s100, s101, 1
	s_lshl_b64 vcc, 1, s101
	s_mov_b64 exec, vcc
	v_mov_b32_e32 v98, s42
	s_add_u32 s42, s8, s42
	s_addc_u32 s43, s9, s43
	s_add_i32 s18, s10, 0
	s_add_i32 s18, s18, 0x23000
	v_mov_b32_e32 v2, s18

.LBB0_1266:
	s_cmp_ge_i32 s18, s27
	s_mov_b64 s[6:7], -1
	s_cbranch_scc1 .LBB0_1258
	s_and_saveexec_b64 s[6:7], s[38:39]
	s_cbranch_execz .LBB0_1257
	s_sub_i32 s40, s18, s21
	s_addk_i32 s40, 0x240
	s_cmp_lt_i32 s18, s21
	s_cselect_b32 s40, s18, s40
	s_ashr_i32 s41, s40, 31
	s_lshl_b64 s[40:41], s[40:41], 2
	s_lshr_b32 s101, s10, 2
	s_add_i32 s101, s101, 1
	s_add_i32 s100, s101, 1
	s_lshl_b64 vcc, 1, s101
	s_mov_b64 exec, vcc
	v_mov_b32_e32 v98, s40
	s_add_u32 s40, s8, s40
	s_addc_u32 s41, s9, s41
	s_add_i32 s18, s10, 0
	s_add_i32 s18, s18, 0x23004
	v_mov_b32_e32 v2, s18
	s_branch .LBB0_1257
.LBB0_1269:
	v_cmp_gt_u32_e32 vcc, s100, v14
	v_lshlrev_b32_e32 v99, 2, v14
	v_add_u32_e32 v99, 0x23000, v99
	s_and_saveexec_b64 s[100:101], vcc
	global_load_dword v97, v98, s[8:9]
	s_waitcnt vmcnt(0)
	ds_write_b32 v99, v97
	s_mov_b64 exec, s[100:101]
	v_readlane_b32 s6, v253, 61
	v_readlane_b32 s7, v253, 62
	s_waitcnt lgkmcnt(0)
	s_barrier
	s_movk_i32 s38, 0x200
	v_readfirstlane_b32 s48, v14
	s_and_b64 vcc, exec, s[6:7]
	s_cbranch_vccz .LBB0_1312
	s_ashr_i32 s6, s20, 31
	s_lshr_b32 s6, s6, 29
	s_add_i32 s6, s20, s6
	s_ashr_i32 s8, s6, 3
	s_and_b32 s6, s6, -8
	s_sub_i32 s18, s20, s6
	s_cbranch_execnz .LBB0_1272
